# speedup vs baseline: 1.0129x; 1.0005x over previous
.LBB1_4:
	s_or_b64 exec, exec, s[10:11]
	s_waitcnt lgkmcnt(0)
	v_lshrrev_b32_e32 v103, 4, v0
	v_bfe_u32 v104, v0, 3, 2
	v_lshlrev_b32_e32 v102, 4, v0
	v_and_or_b32 v103, v103, 4, v104
	v_lshl_add_u32 v105, v107, 2, 0
	v_lshlrev_b32_e32 v103, 6, v103
	v_and_b32_e32 v102, 48, v102
	s_barrier
	ds_read2st64_b32 v[98:99], v105 offset0:128 offset1:129
	ds_read2st64_b32 v[100:101], v105 offset0:132 offset1:133
	v_add3_u32 v109, 0, v103, v102
	ds_read2st64_b32 v[102:103], v105 offset0:134 offset1:135
	ds_read2st64_b32 v[104:105], v105 offset0:130 offset1:131
	s_movk_i32 s4, 0x70
	v_lshrrev_b32_e32 v108, 5, v146
	s_waitcnt vmcnt(17) lgkmcnt(2)
	v_fma_f32 v22, v22, v99, v101
	v_fma_f32 v23, v23, v99, v101
	s_waitcnt vmcnt(15) lgkmcnt(0)
	v_fma_f32 v14, v14, v104, v102
	v_fma_f32 v15, v15, v104, v102
	v_cvt_pk_bf16_f32 v22, v22, v23
	v_fma_f32 v23, v24, v99, v101
	v_fma_f32 v24, v25, v99, v101
	v_fma_f32 v18, v18, v99, v101
	v_fma_f32 v19, v19, v99, v101
	v_cvt_pk_bf16_f32 v14, v14, v15
	v_fma_f32 v15, v16, v104, v102
	v_fma_f32 v16, v17, v104, v102
	s_waitcnt vmcnt(14)
	v_fma_f32 v10, v10, v104, v102
	v_fma_f32 v11, v11, v104, v102
	s_waitcnt vmcnt(13)
	v_fma_f32 v6, v6, v105, v103
	v_fma_f32 v7, v7, v105, v103
	v_fma_f32 v30, v30, v98, v100
	v_fma_f32 v31, v31, v98, v100
	v_fma_f32 v32, v32, v98, v100
	v_fma_f32 v33, v33, v98, v100
	v_fma_f32 v26, v26, v98, v100
	v_fma_f32 v27, v27, v98, v100
	v_cvt_pk_bf16_f32 v23, v23, v24
	v_cvt_pk_bf16_f32 v24, v18, v19
	v_fma_f32 v18, v20, v99, v101
	v_fmac_f32_e32 v101, v21, v99
	v_cvt_pk_bf16_f32 v15, v15, v16
	v_cvt_pk_bf16_f32 v16, v10, v11
	v_fma_f32 v10, v12, v104, v102
	v_fma_f32 v11, v13, v104, v102
	v_cvt_pk_bf16_f32 v6, v6, v7
	v_fma_f32 v7, v8, v105, v103
	v_fma_f32 v8, v9, v105, v103
	s_waitcnt vmcnt(12)
	v_fma_f32 v2, v2, v105, v103
	v_fma_f32 v3, v3, v105, v103
	v_cvt_pk_bf16_f32 v30, v30, v31
	v_cvt_pk_bf16_f32 v31, v32, v33
	v_cvt_pk_bf16_f32 v32, v26, v27
	v_fma_f32 v26, v28, v98, v100
	v_fma_f32 v27, v29, v98, v100
	v_cvt_pk_bf16_f32 v25, v18, v101
	v_bitop3_b32 v18, v107, s4, 64 bitop3:0xc8
	v_cvt_pk_bf16_f32 v17, v10, v11
	s_movk_i32 s4, 0xb0
	v_mov_b32_e32 v10, 0x80
	v_cvt_pk_bf16_f32 v7, v7, v8
	v_cvt_pk_bf16_f32 v8, v2, v3
	v_fma_f32 v2, v4, v105, v103
	v_fmac_f32_e32 v103, v5, v105
	v_cvt_pk_bf16_f32 v33, v26, v27
	v_lshlrev_b32_e32 v27, 1, v107
	v_bitop3_b32 v10, v107, s4, v10 bitop3:0xc8
	v_cvt_pk_bf16_f32 v9, v2, v103
	s_movk_i32 s4, 0xf0
	v_mov_b32_e32 v2, 0xc0
	v_and_b32_e32 v26, 48, v107
	v_and_b32_e32 v27, 8, v27
	v_bitop3_b32 v2, v107, s4, v2 bitop3:0xc8
	v_or3_b32 v26, v26, v27, v106
	v_or3_b32 v18, v18, v27, v106
	v_or3_b32 v10, v10, v27, v106
	v_or3_b32 v2, v2, v27, v106
	v_lshlrev_b32_e32 v26, 7, v26
	v_lshlrev_b32_e32 v18, 7, v18
	v_lshlrev_b32_e32 v10, 7, v10
	v_lshlrev_b32_e32 v2, 7, v2
	v_and_b32_e32 v26, 0x1e00, v26
	v_and_b32_e32 v18, 0x3e00, v18
	v_and_b32_e32 v10, 0x5e00, v10
	v_and_b32_e32 v2, 0x7e00, v2
	v_add_u32_e32 v26, v109, v26
	v_add_u32_e32 v18, v109, v18
	v_add_u32_e32 v10, v109, v10
	v_add_u32_e32 v2, v109, v2
	v_mov_b32_e32 v131, 0
	ds_write_b128 v26, v[30:33]
	ds_write_b128 v18, v[22:25]
	ds_write_b128 v10, v[14:17]
	ds_write_b128 v2, v[6:9]
	v_lshl_add_u64 v[2:3], v[130:131], 2, s[8:9]
	v_lshlrev_b32_e32 v136, 4, v108
	v_mov_b32_e32 v137, v131
	v_lshl_add_u64 v[138:139], v[2:3], 0, v[136:137]
	s_waitcnt lgkmcnt(0)
	s_barrier
	global_load_dwordx4 v[2:5], v[138:139], off
	global_load_dwordx4 v[6:9], v[138:139], off offset:32
	global_load_dwordx4 v[10:13], v[138:139], off offset:64
	global_load_dwordx4 v[14:17], v[138:139], off offset:96
	v_lshlrev_b32_e32 v18, 3, v146
	v_and_b32_e32 v19, 24, v18
	v_and_b32_e32 v20, 0xc0, v134
	v_lshlrev_b32_e32 v21, 1, v0
	v_and_b32_e32 v21, 32, v21
	v_and_b32_e32 v18, 0x100, v18
	v_add3_u32 v19, 0, v19, v20
	v_add3_u32 v140, v19, v21, v18
	ds_read_b64_tr_b16 v[192:193], v140
	ds_read_b64_tr_b16 v[194:195], v140 offset:1024
	ds_read_b64_tr_b16 v[196:197], v140 offset:2048
	ds_read_b64_tr_b16 v[198:199], v140 offset:3072
	ds_read_b64_tr_b16 v[200:201], v140 offset:4096
	ds_read_b64_tr_b16 v[202:203], v140 offset:5120
	ds_read_b64_tr_b16 v[204:205], v140 offset:512
	ds_read_b64_tr_b16 v[206:207], v140 offset:1536
	s_waitcnt vmcnt(0)
	s_waitcnt lgkmcnt(6)
	v_mfma_f32_32x32x16_bf16 v[18:33], v[94:97], v[192:195], v[2:17]
	ds_read_b64_tr_b16 v[192:193], v140 offset:6144
	ds_read_b64_tr_b16 v[194:195], v140 offset:7168
	s_mov_b32 s4, 0x20000
	v_and_b32_e32 v137, 31, v0
	s_waitcnt lgkmcnt(6)
	v_mfma_f32_32x32x16_bf16 v[18:33], v[86:89], v[196:199], v[18:33]
	ds_read_b64_tr_b16 v[196:197], v140 offset:2560
	ds_read_b64_tr_b16 v[198:199], v140 offset:3584
	s_waitcnt lgkmcnt(6)
	v_mfma_f32_32x32x16_bf16 v[18:33], v[54:57], v[200:203], v[18:33]
	ds_read_b64_tr_b16 v[200:201], v140 offset:8192
	ds_read_b64_tr_b16 v[202:203], v140 offset:9216
	s_waitcnt lgkmcnt(6)
	v_mfma_f32_32x32x16_bf16 v[2:17], v[94:97], v[204:207], v[2:17]
	ds_read_b64_tr_b16 v[204:205], v140 offset:4608
	ds_read_b64_tr_b16 v[206:207], v140 offset:5632
	s_waitcnt lgkmcnt(6)
	v_mfma_f32_32x32x16_bf16 v[18:33], v[42:45], v[192:195], v[18:33]
	ds_read_b64_tr_b16 v[192:193], v140 offset:10240
	ds_read_b64_tr_b16 v[194:195], v140 offset:11264
	s_waitcnt lgkmcnt(6)
	v_mfma_f32_32x32x16_bf16 v[2:17], v[86:89], v[196:199], v[2:17]
	ds_read_b64_tr_b16 v[196:197], v140 offset:6656
	ds_read_b64_tr_b16 v[198:199], v140 offset:7680
	s_waitcnt lgkmcnt(6)
	v_mfma_f32_32x32x16_bf16 v[18:33], v[90:93], v[200:203], v[18:33]
	ds_read_b64_tr_b16 v[200:201], v140 offset:12288
	ds_read_b64_tr_b16 v[202:203], v140 offset:13312
	s_waitcnt lgkmcnt(6)
	v_mfma_f32_32x32x16_bf16 v[2:17], v[54:57], v[204:207], v[2:17]
	ds_read_b64_tr_b16 v[204:205], v140 offset:8704
	ds_read_b64_tr_b16 v[206:207], v140 offset:9728
	s_waitcnt lgkmcnt(6)
	v_mfma_f32_32x32x16_bf16 v[18:33], v[78:81], v[192:195], v[18:33]
	ds_read_b64_tr_b16 v[192:193], v140 offset:14336
	ds_read_b64_tr_b16 v[194:195], v140 offset:15360
	s_waitcnt lgkmcnt(6)
	v_mfma_f32_32x32x16_bf16 v[2:17], v[42:45], v[196:199], v[2:17]
	ds_read_b64_tr_b16 v[196:197], v140 offset:10752
	ds_read_b64_tr_b16 v[198:199], v140 offset:11776
	s_waitcnt lgkmcnt(6)
	v_mfma_f32_32x32x16_bf16 v[18:33], v[82:85], v[200:203], v[18:33]
	ds_read_b64_tr_b16 v[200:201], v140 offset:16384
	ds_read_b64_tr_b16 v[202:203], v140 offset:17408
	s_waitcnt lgkmcnt(6)
	v_mfma_f32_32x32x16_bf16 v[2:17], v[90:93], v[204:207], v[2:17]
	ds_read_b64_tr_b16 v[204:205], v140 offset:12800
	ds_read_b64_tr_b16 v[206:207], v140 offset:13824
	s_waitcnt lgkmcnt(6)
	v_mfma_f32_32x32x16_bf16 v[18:33], v[74:77], v[192:195], v[18:33]
	ds_read_b64_tr_b16 v[192:193], v140 offset:18432
	ds_read_b64_tr_b16 v[194:195], v140 offset:19456
	s_waitcnt lgkmcnt(6)
	v_mfma_f32_32x32x16_bf16 v[2:17], v[78:81], v[196:199], v[2:17]
	ds_read_b64_tr_b16 v[196:197], v140 offset:14848
	ds_read_b64_tr_b16 v[198:199], v140 offset:15872
	s_waitcnt lgkmcnt(6)
	v_mfma_f32_32x32x16_bf16 v[18:33], v[66:69], v[200:203], v[18:33]
	ds_read_b64_tr_b16 v[200:201], v140 offset:20480
	ds_read_b64_tr_b16 v[202:203], v140 offset:21504
	s_waitcnt lgkmcnt(6)
	v_mfma_f32_32x32x16_bf16 v[2:17], v[82:85], v[204:207], v[2:17]
	ds_read_b64_tr_b16 v[204:205], v140 offset:16896
	ds_read_b64_tr_b16 v[206:207], v140 offset:17920
	s_waitcnt lgkmcnt(6)
	v_mfma_f32_32x32x16_bf16 v[18:33], v[70:73], v[192:195], v[18:33]
	ds_read_b64_tr_b16 v[192:193], v140 offset:22528
	ds_read_b64_tr_b16 v[194:195], v140 offset:23552
	s_waitcnt lgkmcnt(6)
	v_mfma_f32_32x32x16_bf16 v[2:17], v[74:77], v[196:199], v[2:17]
	ds_read_b64_tr_b16 v[196:197], v140 offset:18944
	ds_read_b64_tr_b16 v[198:199], v140 offset:19968
	s_waitcnt lgkmcnt(6)
	v_mfma_f32_32x32x16_bf16 v[18:33], v[62:65], v[200:203], v[18:33]
	ds_read_b64_tr_b16 v[200:201], v140 offset:24576
	ds_read_b64_tr_b16 v[202:203], v140 offset:25600
	s_waitcnt lgkmcnt(6)
	v_mfma_f32_32x32x16_bf16 v[2:17], v[66:69], v[204:207], v[2:17]
	ds_read_b64_tr_b16 v[204:205], v140 offset:20992
	ds_read_b64_tr_b16 v[206:207], v140 offset:22016
	s_waitcnt lgkmcnt(6)
	v_mfma_f32_32x32x16_bf16 v[18:33], v[58:61], v[192:195], v[18:33]
	ds_read_b64_tr_b16 v[192:193], v140 offset:26624
	ds_read_b64_tr_b16 v[194:195], v140 offset:27648
	s_waitcnt lgkmcnt(6)
	v_mfma_f32_32x32x16_bf16 v[2:17], v[70:73], v[196:199], v[2:17]
	ds_read_b64_tr_b16 v[196:197], v140 offset:23040
	ds_read_b64_tr_b16 v[198:199], v140 offset:24064
	s_waitcnt lgkmcnt(6)
	v_mfma_f32_32x32x16_bf16 v[18:33], v[50:53], v[200:203], v[18:33]
	ds_read_b64_tr_b16 v[200:201], v140 offset:28672
	ds_read_b64_tr_b16 v[202:203], v140 offset:29696
	s_waitcnt lgkmcnt(6)
	v_mfma_f32_32x32x16_bf16 v[2:17], v[62:65], v[204:207], v[2:17]
	ds_read_b64_tr_b16 v[204:205], v140 offset:25088
	ds_read_b64_tr_b16 v[206:207], v140 offset:26112
	s_waitcnt lgkmcnt(6)
	v_mfma_f32_32x32x16_bf16 v[18:33], v[46:49], v[192:195], v[18:33]
	ds_read_b64_tr_b16 v[192:193], v140 offset:27136
	ds_read_b64_tr_b16 v[194:195], v140 offset:28160
	s_waitcnt lgkmcnt(6)
	v_mfma_f32_32x32x16_bf16 v[2:17], v[58:61], v[196:199], v[2:17]
	ds_read_b64_tr_b16 v[196:197], v140 offset:29184
	ds_read_b64_tr_b16 v[198:199], v140 offset:30208
	s_waitcnt lgkmcnt(6)
	v_mfma_f32_32x32x16_bf16 v[18:33], v[38:41], v[200:203], v[18:33]
	ds_read_b64_tr_b16 v[200:201], v140 offset:30720
	ds_read_b64_tr_b16 v[202:203], v140 offset:31744
	v_add_co_u32_e64 v42, s[4:5], s4, v132
	s_nop 1
	v_addc_co_u32_e64 v43, s[4:5], 0, v133, s[4:5]
	s_mov_b32 s4, 0x21000
	s_nop 0
	v_add_co_u32_e64 v44, s[4:5], s4, v132
	s_waitcnt lgkmcnt(6)
	v_mfma_f32_32x32x16_bf16 v[2:17], v[50:53], v[204:207], v[2:17]
	ds_read_b64_tr_b16 v[204:205], v140 offset:31232
	ds_read_b64_tr_b16 v[206:207], v140 offset:32256
	s_nop 0
	v_addc_co_u32_e64 v45, s[4:5], 0, v133, s[4:5]
	s_mov_b32 s4, 0x22000
	s_nop 0
	v_add_co_u32_e64 v50, s[4:5], s4, v132
	global_load_dwordx4 v[122:125], v[42:43], off offset:1024
	global_load_dwordx4 v[114:117], v[42:43], off offset:2048
	global_load_dwordx4 v[126:129], v[44:45], off offset:-4096
	global_load_dwordx4 v[110:113], v[44:45], off
	global_load_dwordx4 v[106:109], v[44:45], off offset:1024
	global_load_dwordx4 v[102:105], v[44:45], off offset:2048
	v_addc_co_u32_e64 v51, s[4:5], 0, v133, s[4:5]
	s_mov_b32 s4, 0x23000
	s_nop 0
	v_add_co_u32_e64 v52, s[4:5], s4, v132
	s_waitcnt lgkmcnt(6)
	v_mfma_f32_32x32x16_bf16 v[2:17], v[46:49], v[192:195], v[2:17]
	s_nop 0
	v_addc_co_u32_e64 v53, s[4:5], 0, v133, s[4:5]
	global_load_dwordx4 v[98:101], v[44:45], off offset:3072
	global_load_dwordx4 v[94:97], v[52:53], off offset:-4096
	global_load_dwordx4 v[118:121], v[42:43], off offset:3072
	global_load_dwordx4 v[90:93], v[50:51], off offset:1024
	global_load_dwordx4 v[86:89], v[50:51], off offset:2048
	global_load_dwordx4 v[82:85], v[50:51], off offset:3072
	global_load_dwordx4 v[70:73], v[52:53], off
	global_load_dwordx4 v[66:69], v[52:53], off offset:1024
	global_load_dwordx4 v[74:77], v[52:53], off offset:2048
	global_load_dwordx4 v[78:81], v[52:53], off offset:3072
	s_waitcnt lgkmcnt(4)
	v_mfma_f32_32x32x16_bf16 v[2:17], v[38:41], v[196:199], v[2:17]
	s_barrier
	s_waitcnt lgkmcnt(2)
	v_mfma_f32_32x32x16_bf16 v[18:33], v[34:37], v[200:203], v[18:33]
	v_lshl_add_u32 v38, v137, 2, 0
	s_waitcnt lgkmcnt(0)
	v_mfma_f32_32x32x16_bf16 v[2:17], v[34:37], v[204:207], v[2:17]
	s_nop 9
	v_max3_f32 v39, |v18|, 0, |v19|
	v_max3_f32 v39, v39, |v20|, |v21|
	v_max3_f32 v39, v39, |v22|, |v23|
	v_max3_f32 v39, v39, |v24|, |v25|
	v_max3_f32 v39, v39, |v26|, |v27|
	v_max3_f32 v39, v39, |v28|, |v29|
	v_max3_f32 v34, v39, |v30|, |v31|
	v_max3_f32 v36, |v2|, 0, |v3|
	v_max3_f32 v36, v36, |v4|, |v5|
	v_max3_f32 v36, v36, |v6|, |v7|
	v_max3_f32 v36, v36, |v8|, |v9|
	v_max3_f32 v36, v36, |v10|, |v11|
	v_max3_f32 v36, v36, |v12|, |v13|
	v_max3_f32 v36, v36, |v14|, |v15|
	v_max3_f32 v34, v34, |v32|, |v33|
	v_max3_f32 v36, v36, |v16|, |v17|
	v_mov_b32_e32 v35, v34
	v_mov_b32_e32 v37, v36
	s_nop 0
	v_permlane32_swap_b32_e32 v34, v35
	v_permlane32_swap_b32_e32 v36, v37
	s_and_saveexec_b64 s[4:5], vcc
	s_cbranch_execz .LBB1_6
	v_max_f32_e32 v34, v34, v34
	v_max_f32_e32 v35, v35, v35
	v_max_f32_e32 v34, v34, v35
	v_and_b32_e32 v35, 0x1c0, v0
	v_max_f32_e32 v36, v36, v36
	v_max_f32_e32 v37, v37, v37
	v_lshl_add_u32 v35, v35, 2, v38
	v_max_f32_e32 v36, v36, v37
	v_add_u32_e32 v35, 0x8800, v35
	ds_write2_b32 v35, v34, v36 offset1:32

.LBB1_10:
	s_or_b64 exec, exec, s[14:15]
	global_load_dwordx4 v[34:37], v[138:139], off offset:1024
	global_load_dwordx4 v[38:41], v[138:139], off offset:1056
	global_load_dwordx4 v[42:45], v[138:139], off offset:1088
	global_load_dwordx4 v[46:49], v[138:139], off offset:1120
	ds_read_b64_tr_b16 v[148:149], v140
	ds_read_b64_tr_b16 v[150:151], v140 offset:1024
	ds_read_b64_tr_b16 v[154:155], v140 offset:1536
	ds_read_b64_tr_b16 v[152:153], v140 offset:512
	v_cmp_eq_u32_e32 vcc, 0, v146
	v_rcp_f32_e32 v138, v147
	s_mov_b32 s4, 0x40000
	s_mov_b32 s20, 0x41000
	s_lshl_b64 s[14:15], s[6:7], 20
	s_lshl_b32 s19, s3, 8
	s_add_u32 s14, s10, s14
	s_mov_b32 s17, 0xc0c0400
	s_mov_b32 s18, 0x4000c0c
	ds_read_b64_tr_b16 v[192:193], v140
	ds_read_b64_tr_b16 v[194:195], v140 offset:1024
	ds_read_b64_tr_b16 v[196:197], v140 offset:512
	ds_read_b64_tr_b16 v[198:199], v140 offset:1536
	ds_read_b64_tr_b16 v[200:201], v140 offset:2048
	ds_read_b64_tr_b16 v[202:203], v140 offset:3072
	ds_read_b64_tr_b16 v[204:205], v140 offset:2560
	ds_read_b64_tr_b16 v[206:207], v140 offset:3584
	s_waitcnt vmcnt(0)
	s_waitcnt lgkmcnt(6)
	v_mfma_f32_32x32x16_bf16 v[50:65], v[126:129], v[192:195], v[34:49]
	ds_read_b64_tr_b16 v[192:193], v140 offset:4096
	ds_read_b64_tr_b16 v[194:195], v140 offset:5120
	s_waitcnt lgkmcnt(6)
	v_mfma_f32_32x32x16_bf16 v[34:49], v[126:129], v[196:199], v[34:49]
	ds_read_b64_tr_b16 v[196:197], v140 offset:4608
	ds_read_b64_tr_b16 v[198:199], v140 offset:5632
	s_waitcnt lgkmcnt(6)
	v_mfma_f32_32x32x16_bf16 v[50:65], v[122:125], v[200:203], v[50:65]
	ds_read_b64_tr_b16 v[200:201], v140 offset:6144
	ds_read_b64_tr_b16 v[202:203], v140 offset:7168
	s_waitcnt lgkmcnt(6)
	v_mfma_f32_32x32x16_bf16 v[34:49], v[122:125], v[204:207], v[34:49]
	ds_read_b64_tr_b16 v[204:205], v140 offset:6656
	ds_read_b64_tr_b16 v[206:207], v140 offset:7680
	s_waitcnt lgkmcnt(6)
	v_mfma_f32_32x32x16_bf16 v[50:65], v[114:117], v[192:195], v[50:65]
	ds_read_b64_tr_b16 v[192:193], v140 offset:8192
	ds_read_b64_tr_b16 v[194:195], v140 offset:9216
	s_waitcnt lgkmcnt(6)
	v_mfma_f32_32x32x16_bf16 v[34:49], v[114:117], v[196:199], v[34:49]
	ds_read_b64_tr_b16 v[196:197], v140 offset:8704
	ds_read_b64_tr_b16 v[198:199], v140 offset:9728
	v_rcp_f32_e32 v128, v135
	v_lshlrev_b32_e32 v126, 11, v1
	v_mov_b32_e32 v127, 0
	v_mov_b32_e32 v135, v127
	v_mov_b32_e32 v129, 0x4b400000
	s_waitcnt lgkmcnt(6)
	v_mfma_f32_32x32x16_bf16 v[50:65], v[118:121], v[200:203], v[50:65]
	ds_read_b64_tr_b16 v[200:201], v140 offset:10240
	ds_read_b64_tr_b16 v[202:203], v140 offset:11264
	s_waitcnt lgkmcnt(6)
	v_mfma_f32_32x32x16_bf16 v[34:49], v[118:121], v[204:207], v[34:49]
	ds_read_b64_tr_b16 v[204:205], v140 offset:10752
	ds_read_b64_tr_b16 v[206:207], v140 offset:11776
	s_waitcnt lgkmcnt(6)
	v_mfma_f32_32x32x16_bf16 v[50:65], v[110:113], v[192:195], v[50:65]
	ds_read_b64_tr_b16 v[192:193], v140 offset:12288
	ds_read_b64_tr_b16 v[194:195], v140 offset:13312
	s_waitcnt lgkmcnt(6)
	v_mfma_f32_32x32x16_bf16 v[34:49], v[110:113], v[196:199], v[34:49]
	ds_read_b64_tr_b16 v[196:197], v140 offset:12800
	ds_read_b64_tr_b16 v[198:199], v140 offset:13824
	s_waitcnt lgkmcnt(6)
	v_mfma_f32_32x32x16_bf16 v[50:65], v[106:109], v[200:203], v[50:65]
	ds_read_b64_tr_b16 v[200:201], v140 offset:14336
	ds_read_b64_tr_b16 v[202:203], v140 offset:15360
	s_waitcnt lgkmcnt(6)
	v_mfma_f32_32x32x16_bf16 v[34:49], v[106:109], v[204:207], v[34:49]
	ds_read_b64_tr_b16 v[204:205], v140 offset:14848
	ds_read_b64_tr_b16 v[206:207], v140 offset:15872
	s_waitcnt lgkmcnt(6)
	v_mfma_f32_32x32x16_bf16 v[50:65], v[102:105], v[192:195], v[50:65]
	ds_read_b64_tr_b16 v[192:193], v140 offset:16384
	ds_read_b64_tr_b16 v[194:195], v140 offset:17408
	s_waitcnt lgkmcnt(6)
	v_mfma_f32_32x32x16_bf16 v[34:49], v[102:105], v[196:199], v[34:49]
	ds_read_b64_tr_b16 v[196:197], v140 offset:16896
	ds_read_b64_tr_b16 v[198:199], v140 offset:17920
	s_waitcnt lgkmcnt(6)
	v_mfma_f32_32x32x16_bf16 v[50:65], v[98:101], v[200:203], v[50:65]
	ds_read_b64_tr_b16 v[200:201], v140 offset:18432
	ds_read_b64_tr_b16 v[202:203], v140 offset:19456
	s_waitcnt lgkmcnt(6)
	v_mfma_f32_32x32x16_bf16 v[34:49], v[98:101], v[204:207], v[34:49]
	ds_read_b64_tr_b16 v[204:205], v140 offset:18944
	ds_read_b64_tr_b16 v[206:207], v140 offset:19968
	s_waitcnt lgkmcnt(6)
	v_mfma_f32_32x32x16_bf16 v[50:65], v[94:97], v[192:195], v[50:65]
	ds_read_b64_tr_b16 v[192:193], v140 offset:20480
	ds_read_b64_tr_b16 v[194:195], v140 offset:21504
	s_waitcnt lgkmcnt(6)
	v_mfma_f32_32x32x16_bf16 v[34:49], v[94:97], v[196:199], v[34:49]
	ds_read_b64_tr_b16 v[196:197], v140 offset:20992
	ds_read_b64_tr_b16 v[198:199], v140 offset:22016
	v_mul_f32_e32 v94, 0x42fe0000, v128
	v_mul_f32_e32 v94, 0x3f7fffff, v94
	v_fmaak_f32 v97, v23, v94, 0x4b400000
	v_fmaak_f32 v95, v19, v94, 0x4b400000
	v_fmaak_f32 v96, v18, v94, 0x4b400000
	v_fmaak_f32 v21, v21, v94, 0x4b400000
	v_fmaak_f32 v20, v20, v94, 0x4b400000
	s_waitcnt lgkmcnt(6)
	v_mfma_f32_32x32x16_bf16 v[50:65], v[90:93], v[200:203], v[50:65]
	ds_read_b64_tr_b16 v[200:201], v140 offset:22528
	ds_read_b64_tr_b16 v[202:203], v140 offset:23552
	v_fmaak_f32 v102, v22, v94, 0x4b400000
	v_add_co_u32_e64 v22, s[4:5], s4, v132
	v_fmaak_f32 v104, v24, v94, 0x4b400000
	s_nop 0
	v_addc_co_u32_e64 v23, s[4:5], 0, v133, s[4:5]
	v_add_co_u32_e64 v24, s[4:5], s20, v132
	s_waitcnt lgkmcnt(6)
	v_mfma_f32_32x32x16_bf16 v[34:49], v[90:93], v[204:207], v[34:49]
	ds_read_b64_tr_b16 v[204:205], v140 offset:23040
	ds_read_b64_tr_b16 v[206:207], v140 offset:24064
	v_fmaak_f32 v103, v25, v94, 0x4b400000
	v_addc_co_u32_e64 v25, s[4:5], 0, v133, s[4:5]
	s_addc_u32 s5, s11, s15
	s_add_u32 s4, s14, s19
	s_addc_u32 s5, s5, 0
	v_lshl_add_u64 v[18:19], s[4:5], 0, v[126:127]
	s_waitcnt lgkmcnt(6)
	v_mfma_f32_32x32x16_bf16 v[50:65], v[86:89], v[192:195], v[50:65]
	ds_read_b64_tr_b16 v[192:193], v140 offset:24576
	ds_read_b64_tr_b16 v[194:195], v140 offset:25600
	v_fmaak_f32 v27, v27, v94, 0x4b400000
	v_fmaak_f32 v26, v26, v94, 0x4b400000
	v_fmaak_f32 v29, v29, v94, 0x4b400000
	v_fmaak_f32 v28, v28, v94, 0x4b400000
	v_fmaak_f32 v31, v31, v94, 0x4b400000
	v_fmaak_f32 v30, v30, v94, 0x4b400000
	v_fmaak_f32 v98, v33, v94, 0x4b400000
	s_waitcnt lgkmcnt(6)
	v_mfma_f32_32x32x16_bf16 v[34:49], v[86:89], v[196:199], v[34:49]
	ds_read_b64_tr_b16 v[196:197], v140 offset:25088
	ds_read_b64_tr_b16 v[198:199], v140 offset:26112
	v_fmaak_f32 v94, v32, v94, 0x4b400000
	v_lshl_add_u64 v[32:33], v[18:19], 0, v[134:135]
	v_perm_b32 v18, v95, v96, s17
	v_perm_b32 v19, v21, v20, s18
	v_perm_b32 v20, v97, v102, s17
	v_perm_b32 v21, v103, v104, s18
	v_or_b32_e32 v18, v18, v19
	s_waitcnt lgkmcnt(6)
	v_mfma_f32_32x32x16_bf16 v[50:65], v[82:85], v[200:203], v[50:65]
	ds_read_b64_tr_b16 v[200:201], v140 offset:26624
	ds_read_b64_tr_b16 v[202:203], v140 offset:27648
	v_or_b32_e32 v19, v20, v21
	v_mul_f32_e32 v20, 0x42fe0000, v138
	v_mul_f32_e32 v126, 0x3f7fffff, v20
	s_mov_b32 s4, 0x42000
	v_perm_b32 v21, v31, v30, s17
	v_fmaak_f32 v128, v3, v126, 0x4b400000
	v_perm_b32 v3, v98, v94, s18
	s_waitcnt lgkmcnt(6)
	v_mfma_f32_32x32x16_bf16 v[34:49], v[82:85], v[204:207], v[34:49]
	ds_read_b64_tr_b16 v[204:205], v140 offset:27136
	ds_read_b64_tr_b16 v[206:207], v140 offset:28160
	v_fmaak_f32 v134, v2, v126, 0x4b400000
	v_add_co_u32_e64 v2, s[4:5], s4, v132
	v_perm_b32 v26, v27, v26, s17
	v_perm_b32 v27, v29, v28, s18
	v_or_b32_e32 v21, v21, v3
	v_addc_co_u32_e64 v3, s[4:5], 0, v133, s[4:5]
	s_waitcnt lgkmcnt(6)
	v_mfma_f32_32x32x16_bf16 v[50:65], v[70:73], v[192:195], v[50:65]
	ds_read_b64_tr_b16 v[192:193], v140 offset:29184
	ds_read_b64_tr_b16 v[194:195], v140 offset:30208
	v_or_b32_e32 v20, v26, v27
	s_mov_b32 s4, 0x43000
	global_load_dwordx4 v[114:117], v[22:23], off offset:1024
	global_load_dwordx4 v[110:113], v[22:23], off offset:2048
	global_load_dwordx4 v[118:121], v[24:25], off offset:-4096
	global_load_dwordx4 v[102:105], v[24:25], off
	v_fmaak_f32 v5, v5, v126, 0x4b400000
	global_store_dwordx4 v[32:33], v[18:21], off
	global_load_dwordx4 v[94:97], v[24:25], off offset:1024
	global_load_dwordx4 v[82:85], v[24:25], off offset:2048
	s_waitcnt lgkmcnt(6)
	v_mfma_f32_32x32x16_bf16 v[34:49], v[70:73], v[196:199], v[34:49]
	ds_read_b64_tr_b16 v[196:197], v140 offset:28672
	ds_read_b64_tr_b16 v[198:199], v140 offset:29696
	v_add_co_u32_e64 v18, s[4:5], s4, v132
	v_fmaak_f32 v4, v4, v126, 0x4b400000
	s_nop 0
	v_addc_co_u32_e64 v19, s[4:5], 0, v133, s[4:5]
	global_load_dwordx4 v[90:93], v[24:25], off offset:3072
	global_load_dwordx4 v[106:109], v[18:19], off offset:-4096
	global_load_dwordx4 v[122:125], v[22:23], off offset:3072
	global_load_dwordx4 v[98:101], v[2:3], off offset:1024
	global_load_dwordx4 v[86:89], v[2:3], off offset:2048
	global_load_dwordx4 v[70:73], v[2:3], off offset:3072
	v_fmaak_f32 v3, v8, v126, 0x4b400000
	s_waitcnt lgkmcnt(6)
	v_mfma_f32_32x32x16_bf16 v[50:65], v[66:69], v[200:203], v[50:65]
	ds_read_b64_tr_b16 v[200:201], v140 offset:31232
	ds_read_b64_tr_b16 v[202:203], v140 offset:32256
	v_fmaak_f32 v8, v11, v126, 0x4b400000
	v_fmaak_f32 v11, v12, v126, 0x4b400000
	v_fmaak_f32 v2, v9, v126, 0x4b400000
	v_fmaak_f32 v9, v10, v126, 0x4b400000
	v_fmaak_f32 v10, v13, v126, 0x4b400000
	v_fmaak_f32 v7, v7, v126, 0x4b400000
	v_fmaak_f32 v6, v6, v126, 0x4b400000
	s_waitcnt lgkmcnt(6)
	v_mfma_f32_32x32x16_bf16 v[34:49], v[66:69], v[204:207], v[34:49]
	ds_read_b64_tr_b16 v[204:205], v140 offset:30720
	ds_read_b64_tr_b16 v[206:207], v140 offset:31744
	global_load_dwordx4 v[28:31], v[18:19], off
	global_load_dwordx4 v[66:69], v[18:19], off offset:1024
	global_load_dwordx4 v[24:27], v[18:19], off offset:2048
	s_nop 0
	global_load_dwordx4 v[18:21], v[18:19], off offset:3072
	v_perm_b32 v4, v5, v4, s18
	v_perm_b32 v5, v7, v6, s17
	v_perm_b32 v2, v2, v3, s18
	v_or_b32_e32 v5, v5, v2
	v_perm_b32 v2, v8, v9, s17
	v_fmaak_f32 v15, v15, v126, 0x4b400000
	s_waitcnt lgkmcnt(6)
	v_mfma_f32_32x32x16_bf16 v[34:49], v[74:77], v[192:195], v[34:49]
	v_fmaak_f32 v14, v14, v126, 0x4b400000
	v_fmac_f32_e32 v129, v16, v126
	v_fmaak_f32 v16, v17, v126, 0x4b400000
	v_perm_b32 v3, v10, v11, s18
	v_perm_b32 v17, v128, v134, s17
	v_or_b32_e32 v4, v17, v4
	s_waitcnt lgkmcnt(4)
	v_mfma_f32_32x32x16_bf16 v[50:65], v[74:77], v[196:199], v[50:65]
	s_waitcnt lgkmcnt(2)
	v_mfma_f32_32x32x16_bf16 v[34:49], v[78:81], v[200:203], v[34:49]
	s_waitcnt lgkmcnt(0)
	v_mfma_f32_32x32x16_bf16 v[50:65], v[78:81], v[204:207], v[50:65]
	s_nop 10
	v_max3_f32 v22, |v34|, 0, |v35|
	v_max3_f32 v22, v22, |v36|, |v37|
	v_max3_f32 v22, v22, |v38|, |v39|
	v_max3_f32 v22, v22, |v40|, |v41|
	v_max3_f32 v22, v22, |v42|, |v43|
	v_max3_f32 v22, v22, |v44|, |v45|
	v_max3_f32 v22, v22, |v46|, |v47|
	v_max3_f32 v12, |v50|, 0, |v51|
	v_max3_f32 v12, v12, |v52|, |v53|
	v_max3_f32 v12, v12, |v54|, |v55|
	v_max3_f32 v12, v12, |v56|, |v57|
	v_max3_f32 v12, v12, |v58|, |v59|
	v_max3_f32 v12, v12, |v60|, |v61|
	v_max3_f32 v22, v22, |v48|, |v49|
	v_max3_f32 v12, v12, |v62|, |v63|
	v_mov_b32_e32 v23, v22
	v_max3_f32 v12, v12, |v64|, |v65|
	s_nop 0
	v_permlane32_swap_b32_e32 v22, v23
	v_mov_b32_e32 v13, v12
	v_max_f32_e32 v23, v23, v23
	v_max_f32_e32 v22, v22, v22
	v_permlane32_swap_b32_e32 v12, v13
	v_max_f32_e32 v22, v22, v23
	v_max3_f32 v12, v12, v13, v22
	v_or_b32_e32 v6, v2, v3
	v_perm_b32 v2, v15, v14, s17
	v_perm_b32 v3, v16, v129, s18
	v_or_b32_e32 v7, v2, v3
	global_store_dwordx4 v[32:33], v[4:7], off offset:1024
	v_max_f32_dpp v12, v12, v12 quad_perm:[1,0,3,2] row_mask:0xf bank_mask:0xf
	s_nop 1
	v_max_f32_dpp v12, v12, v12 quad_perm:[2,3,0,1] row_mask:0xf bank_mask:0xf
	s_nop 1
	v_max_f32_dpp v12, v12, v12 row_half_mirror row_mask:0xf bank_mask:0xf
	s_nop 1
	v_max_f32_dpp v12, v12, v12 row_mirror row_mask:0xf bank_mask:0xf
	v_mov_b32_e32 v13, v12
	s_nop 1
	v_permlane16_swap_b32_e32 v13, v12
	v_max_f32_e32 v2, v13, v12
	s_waitcnt lgkmcnt(0)
	s_barrier
	s_and_saveexec_b64 s[4:5], vcc
	v_lshl_add_u32 v1, v1, 2, 0
	ds_write_b32 v1, v2 offset:34816
	s_or_b64 exec, exec, s[4:5]
	s_waitcnt lgkmcnt(0)
	s_barrier
	ds_read_b128 v[2:5], v127 offset:34816
	ds_read_b128 v[6:9], v127 offset:34832
	s_mov_b32 s4, 0x1e3ce508
	v_cmp_eq_u32_e32 vcc, 0, v0
	s_waitcnt lgkmcnt(1)
	v_max_f32_e32 v1, v2, v2
	v_max_f32_e32 v1, 0, v1
	v_max3_f32 v1, v1, v3, v4
	s_waitcnt lgkmcnt(0)
	v_max3_f32 v1, v1, v5, v6
	v_max3_f32 v1, v1, v7, v8
	v_max3_f32 v1, v1, v9, s4
	s_and_saveexec_b64 s[4:5], vcc
	s_cbranch_execz .LBB1_14
	s_load_dwordx2 s[0:1], s[0:1], 0x40
	s_andn2_b32 s2, s2, 63
	s_lshr_b32 s14, s3, 6
	s_or_b32 s14, s14, s2
	s_ashr_i32 s15, s14, 31
	s_lshl_b64 s[14:15], s[14:15], 2
	s_waitcnt lgkmcnt(0)
	s_add_u32 s0, s0, s14
	s_addc_u32 s1, s1, s15
	v_mov_b32_e32 v2, 0
	v_mul_f32_e32 v3, 0x3c010204, v1
	global_store_dword v2, v3, s[0:1]

	.amdhsa_kernel _Z10qkv_kernelPKfS0_S0_PKdPKtS0_PhPfS6_
		.amdhsa_group_segment_fixed_size 0
		.amdhsa_private_segment_fixed_size 0
		.amdhsa_kernarg_size 72
		.amdhsa_user_sgpr_count 2
		.amdhsa_user_sgpr_dispatch_ptr 0
		.amdhsa_user_sgpr_queue_ptr 0
		.amdhsa_user_sgpr_kernarg_segment_ptr 1
		.amdhsa_user_sgpr_dispatch_id 0
		.amdhsa_user_sgpr_kernarg_preload_length 0
		.amdhsa_user_sgpr_kernarg_preload_offset 0
		.amdhsa_user_sgpr_private_segment_size 0
		.amdhsa_uses_dynamic_stack 0
		.amdhsa_enable_private_segment 0
		.amdhsa_system_sgpr_workgroup_id_x 1
		.amdhsa_system_sgpr_workgroup_id_y 0
		.amdhsa_system_sgpr_workgroup_id_z 0
		.amdhsa_system_sgpr_workgroup_info 0
		.amdhsa_system_vgpr_workitem_id 0
		.amdhsa_next_free_vgpr 208
		.amdhsa_next_free_sgpr 32
		.amdhsa_accum_offset 208
		.amdhsa_reserve_vcc 1
		.amdhsa_float_round_mode_32 0
		.amdhsa_float_round_mode_16_64 0
		.amdhsa_float_denorm_mode_32 3
		.amdhsa_float_denorm_mode_16_64 3
		.amdhsa_dx10_clamp 1
		.amdhsa_ieee_mode 1
		.amdhsa_fp16_overflow 0
		.amdhsa_tg_split 0
		.amdhsa_exception_fp_ieee_invalid_op 0
		.amdhsa_exception_fp_denorm_src 0
		.amdhsa_exception_fp_ieee_div_zero 0
		.amdhsa_exception_fp_ieee_overflow 0
		.amdhsa_exception_fp_ieee_underflow 0
		.amdhsa_exception_fp_ieee_inexact 0
		.amdhsa_exception_int_div_zero 0
	.end_amdhsa_kernel

amdhsa.kernels:
  - .agpr_count:     0
    .args:
      - .actual_access:  read_only
        .address_space:  global
        .offset:         0
        .size:           8
        .value_kind:     global_buffer
      - .actual_access:  read_only
        .address_space:  global
        .offset:         8
        .size:           8
        .value_kind:     global_buffer
      - .actual_access:  read_only
        .address_space:  global
        .offset:         16
        .size:           8
        .value_kind:     global_buffer
      - .actual_access:  write_only
        .address_space:  global
        .offset:         24
        .size:           8
        .value_kind:     global_buffer
      - .actual_access:  write_only
        .address_space:  global
        .offset:         32
        .size:           8
        .value_kind:     global_buffer
      - .actual_access:  write_only
        .address_space:  global
        .offset:         40
        .size:           8
        .value_kind:     global_buffer
    .group_segment_fixed_size: 512
    .kernarg_segment_align: 8
    .kernarg_segment_size: 48
    .language:       OpenCL C
    .language_version:
      - 2
      - 0
    .max_flat_workgroup_size: 1024
    .name:           _Z11prep_kernelPKfS0_S0_PdPtS2_
    .private_segment_fixed_size: 0
    .sgpr_count:     26
    .sgpr_spill_count: 0
    .symbol:         _Z11prep_kernelPKfS0_S0_PdPtS2_.kd
    .uniform_work_group_size: 1
    .uses_dynamic_stack: false
    .vgpr_count:     32
    .vgpr_spill_count: 0
    .wavefront_size: 64
  - .agpr_count:     0
    .args:
      - .actual_access:  read_only
        .address_space:  global
        .offset:         0
        .size:           8
        .value_kind:     global_buffer
      - .actual_access:  read_only
        .address_space:  global
        .offset:         8
        .size:           8
        .value_kind:     global_buffer
      - .actual_access:  read_only
        .address_space:  global
        .offset:         16
        .size:           8
        .value_kind:     global_buffer
      - .actual_access:  read_only
        .address_space:  global
        .offset:         24
        .size:           8
        .value_kind:     global_buffer
      - .actual_access:  read_only
        .address_space:  global
        .offset:         32
        .size:           8
        .value_kind:     global_buffer
      - .actual_access:  read_only
        .address_space:  global
        .offset:         40
        .size:           8
        .value_kind:     global_buffer
      - .actual_access:  write_only
        .address_space:  global
        .offset:         48
        .size:           8
        .value_kind:     global_buffer
      - .actual_access:  write_only
        .address_space:  global
        .offset:         56
        .size:           8
        .value_kind:     global_buffer
      - .actual_access:  write_only
        .address_space:  global
        .offset:         64
        .size:           8
        .value_kind:     global_buffer
    .group_segment_fixed_size: 0
    .kernarg_segment_align: 8
    .kernarg_segment_size: 72
    .language:       OpenCL C
    .language_version:
      - 2
      - 0
    .max_flat_workgroup_size: 512
    .name:           _Z10qkv_kernelPKfS0_S0_PKdPKtS0_PhPfS6_
    .private_segment_fixed_size: 0
    .sgpr_count:     38
    .sgpr_spill_count: 0
    .symbol:         _Z10qkv_kernelPKfS0_S0_PKdPKtS0_PhPfS6_.kd
    .uniform_work_group_size: 1
    .uses_dynamic_stack: false
    .vgpr_count:     208
    .vgpr_spill_count: 0
    .wavefront_size: 64
  - .agpr_count:     0
    .args:
      - .actual_access:  read_only
        .address_space:  global
        .offset:         0
        .size:           8
        .value_kind:     global_buffer
      - .address_space:  global
        .offset:         8
        .size:           8
        .value_kind:     global_buffer
      - .address_space:  global
        .offset:         16
        .size:           8
        .value_kind:     global_buffer
      - .actual_access:  read_only
        .address_space:  global
        .offset:         24
        .size:           8
        .value_kind:     global_buffer
      - .actual_access:  read_only
        .address_space:  global
        .offset:         32
        .size:           8
        .value_kind:     global_buffer
      - .actual_access:  write_only
        .address_space:  global
        .offset:         40
        .size:           8
        .value_kind:     global_buffer
      - .actual_access:  write_only
        .address_space:  global
        .offset:         48
        .size:           8
        .value_kind:     global_buffer
      - .actual_access:  write_only
        .address_space:  global
        .offset:         56
        .size:           8
        .value_kind:     global_buffer
    .group_segment_fixed_size: 0
    .kernarg_segment_align: 8
    .kernarg_segment_size: 64
    .language:       OpenCL C
    .language_version:
      - 2
      - 0
    .max_flat_workgroup_size: 512
    .name:           _Z11attn_kernelPKhS0_S0_PKfS2_PhPfS4_
    .private_segment_fixed_size: 0
    .sgpr_count:     72
    .sgpr_spill_count: 0
    .symbol:         _Z11attn_kernelPKhS0_S0_PKfS2_PhPfS4_.kd
    .uniform_work_group_size: 1
    .uses_dynamic_stack: false
    .vgpr_count:     256
    .vgpr_spill_count: 0
    .wavefront_size: 64
  - .agpr_count:     0
    .args:
      - .actual_access:  read_only
        .address_space:  global
        .offset:         0
        .size:           8
        .value_kind:     global_buffer
      - .actual_access:  read_only
        .address_space:  global
        .offset:         8
        .size:           8
        .value_kind:     global_buffer
      - .actual_access:  read_only
        .address_space:  global
        .offset:         16
        .size:           8
        .value_kind:     global_buffer
      - .actual_access:  read_only
        .address_space:  global
        .offset:         24
        .size:           8
        .value_kind:     global_buffer
      - .actual_access:  read_only
        .address_space:  global
        .offset:         32
        .size:           8
        .value_kind:     global_buffer
      - .actual_access:  read_only
        .address_space:  global
        .offset:         40
        .size:           8
        .value_kind:     global_buffer
      - .actual_access:  write_only
        .address_space:  global
        .offset:         48
        .size:           8
        .value_kind:     global_buffer
    .group_segment_fixed_size: 16640
    .kernarg_segment_align: 8
    .kernarg_segment_size: 56
    .language:       OpenCL C
    .language_version:
      - 2
      - 0
    .max_flat_workgroup_size: 512
    .name:           _Z14outproj_kernelPKhPKfS2_PKtS2_S2_Pf
    .private_segment_fixed_size: 0
    .sgpr_count:     26
    .sgpr_spill_count: 0
    .symbol:         _Z14outproj_kernelPKhPKfS2_PKtS2_S2_Pf.kd
    .uniform_work_group_size: 1
    .uses_dynamic_stack: false
    .vgpr_count:     109
    .vgpr_spill_count: 0
    .wavefront_size: 64
